# gate epilogue: v_ashr_pk_u8_i32 saturating pack replaces ashr+med3+shift/or pack
# baseline (speedup 1.0000x reference)
.LBB0_853:
	s_waitcnt lgkmcnt(0)
	v_fmamk_f32 v160, v160, 0xbfb8aa3b, v184
	v_fmamk_f32 v161, v161, 0xbfb8aa3b, v185
	v_fmamk_f32 v162, v162, 0xbfb8aa3b, v186
	v_fmamk_f32 v163, v163, 0xbfb8aa3b, v187
	v_fmamk_f32 v156, v156, 0xbfb8aa3b, v180
	v_fmamk_f32 v157, v157, 0xbfb8aa3b, v181
	v_fmamk_f32 v158, v158, 0xbfb8aa3b, v182
	v_fmamk_f32 v159, v159, 0xbfb8aa3b, v183
	v_fmamk_f32 v152, v152, 0xbfb8aa3b, v188
	v_fmamk_f32 v153, v153, 0xbfb8aa3b, v189
	v_fmamk_f32 v154, v154, 0xbfb8aa3b, v190
	v_fmamk_f32 v155, v155, 0xbfb8aa3b, v191
	v_fmamk_f32 v148, v148, 0xbfb8aa3b, v192
	v_fmamk_f32 v149, v149, 0xbfb8aa3b, v193
	v_fmamk_f32 v150, v150, 0xbfb8aa3b, v194
	v_fmamk_f32 v151, v151, 0xbfb8aa3b, v195
	v_mov_b32_e32 v223, 0
	s_add_i32 s19, s87, -11
	s_lshr_b32 s20, s19, 2
	v_mov_b32_e32 v184, s20
	v_mov_b32_e32 v185, v3
	v_mad_i64_i32 v[184:185], s[20:21], v220, 3, v[184:185]
	v_lshlrev_b64 v[184:185], 10, v[184:185]
	s_lshl_b32 s19, s19, 8
	s_and_b32 s34, s19, 0x300
	v_lshl_add_u64 v[184:185], s[46:47], 0, v[184:185]
	v_lshl_add_u64 v[184:185], v[184:185], 0, s[34:35]
	v_lshl_add_u64 v[186:187], v[184:185], 0, v[2:3]
	v_exp_f32_e32 v160, v160
	v_exp_f32_e32 v161, v161
	v_exp_f32_e32 v162, v162
	v_exp_f32_e32 v163, v163
	v_exp_f32_e32 v156, v156
	v_exp_f32_e32 v157, v157
	v_exp_f32_e32 v158, v158
	v_exp_f32_e32 v159, v159
	v_exp_f32_e32 v152, v152
	v_exp_f32_e32 v153, v153
	v_exp_f32_e32 v154, v154
	v_exp_f32_e32 v155, v155
	v_exp_f32_e32 v148, v148
	v_exp_f32_e32 v149, v149
	v_exp_f32_e32 v150, v150
	v_exp_f32_e32 v151, v151
	v_add_f32_e32 v160, 1.0, v160
	v_add_f32_e32 v161, 1.0, v161
	v_add_f32_e32 v162, 1.0, v162
	v_add_f32_e32 v163, 1.0, v163
	v_add_f32_e32 v156, 1.0, v156
	v_add_f32_e32 v157, 1.0, v157
	v_add_f32_e32 v158, 1.0, v158
	v_add_f32_e32 v159, 1.0, v159
	v_add_f32_e32 v152, 1.0, v152
	v_add_f32_e32 v153, 1.0, v153
	v_add_f32_e32 v154, 1.0, v154
	v_add_f32_e32 v155, 1.0, v155
	v_add_f32_e32 v148, 1.0, v148
	v_add_f32_e32 v149, 1.0, v149
	v_add_f32_e32 v150, 1.0, v150
	v_add_f32_e32 v151, 1.0, v151
	v_rcp_f32_e32 v160, v160
	v_rcp_f32_e32 v161, v161
	v_rcp_f32_e32 v162, v162
	v_rcp_f32_e32 v163, v163
	v_rcp_f32_e32 v156, v156
	v_rcp_f32_e32 v157, v157
	v_rcp_f32_e32 v158, v158
	v_rcp_f32_e32 v159, v159
	v_rcp_f32_e32 v152, v152
	v_rcp_f32_e32 v153, v153
	v_rcp_f32_e32 v154, v154
	v_rcp_f32_e32 v155, v155
	v_rcp_f32_e32 v148, v148
	v_rcp_f32_e32 v149, v149
	v_rcp_f32_e32 v150, v150
	v_rcp_f32_e32 v151, v151
	v_add_u32_e32 v160, 0xc4820000, v160
	v_add_u32_e32 v161, 0xc4820000, v161
	v_add_u32_e32 v162, 0xc4820000, v162
	v_add_u32_e32 v163, 0xc4820000, v163
	v_add_u32_e32 v156, 0xc4820000, v156
	v_add_u32_e32 v157, 0xc4820000, v157
	v_add_u32_e32 v158, 0xc4820000, v158
	v_add_u32_e32 v159, 0xc4820000, v159
	v_add_u32_e32 v152, 0xc4820000, v152
	v_add_u32_e32 v153, 0xc4820000, v153
	v_add_u32_e32 v154, 0xc4820000, v154
	v_add_u32_e32 v155, 0xc4820000, v155
	v_add_u32_e32 v148, 0xc4820000, v148
	v_add_u32_e32 v149, 0xc4820000, v149
	v_add_u32_e32 v150, 0xc4820000, v150
	v_add_u32_e32 v151, 0xc4820000, v151
	v_ashr_pk_u8_i32 v160, v160, v161, 18
	v_ashr_pk_u8_i32 v162, v162, v163, 18
	v_ashr_pk_u8_i32 v156, v156, v157, 18
	v_ashr_pk_u8_i32 v158, v158, v159, 18
	v_ashr_pk_u8_i32 v152, v152, v153, 18
	v_ashr_pk_u8_i32 v154, v154, v155, 18
	v_ashr_pk_u8_i32 v148, v148, v149, 18
	v_ashr_pk_u8_i32 v150, v150, v151, 18
	v_and_b32_e32 v160, 0xffff, v160
	v_lshl_or_b32 v180, v162, 16, v160
	v_and_b32_e32 v156, 0xffff, v156
	v_lshl_or_b32 v181, v158, 16, v156
	v_and_b32_e32 v152, 0xffff, v152
	v_lshl_or_b32 v182, v154, 16, v152
	v_and_b32_e32 v148, 0xffff, v148
	v_lshl_or_b32 v183, v150, 16, v148
	global_store_dwordx4 v[186:187], v[180:183], off
	s_and_b64 vcc, exec, s[40:41]
	s_mov_b64 s[26:27], -1
	s_cbranch_vccz .LBB0_925

.LBB0_855:
	s_waitcnt lgkmcnt(0)
	v_fmamk_f32 v128, v128, 0xbfb8aa3b, v168
	v_fmamk_f32 v129, v129, 0xbfb8aa3b, v169
	v_fmamk_f32 v130, v130, 0xbfb8aa3b, v170
	v_fmamk_f32 v131, v131, 0xbfb8aa3b, v171
	v_fmamk_f32 v124, v124, 0xbfb8aa3b, v164
	v_fmamk_f32 v125, v125, 0xbfb8aa3b, v165
	v_fmamk_f32 v126, v126, 0xbfb8aa3b, v166
	v_fmamk_f32 v127, v127, 0xbfb8aa3b, v167
	v_fmamk_f32 v120, v120, 0xbfb8aa3b, v172
	v_fmamk_f32 v121, v121, 0xbfb8aa3b, v173
	v_fmamk_f32 v122, v122, 0xbfb8aa3b, v174
	v_fmamk_f32 v123, v123, 0xbfb8aa3b, v175
	v_fmamk_f32 v116, v116, 0xbfb8aa3b, v176
	v_fmamk_f32 v117, v117, 0xbfb8aa3b, v177
	v_fmamk_f32 v118, v118, 0xbfb8aa3b, v178
	v_fmamk_f32 v119, v119, 0xbfb8aa3b, v179
	v_mov_b32_e32 v150, v223
	s_add_i32 s19, s87, -11
	s_lshr_b32 s20, s19, 2
	v_mov_b32_e32 v168, s20
	v_mov_b32_e32 v169, v3
	v_mad_i64_i32 v[168:169], s[20:21], v226, 3, v[168:169]
	v_lshlrev_b64 v[168:169], 10, v[168:169]
	s_lshl_b32 s19, s19, 8
	s_and_b32 s34, s19, 0x300
	v_lshl_add_u64 v[168:169], s[46:47], 0, v[168:169]
	v_lshl_add_u64 v[168:169], v[168:169], 0, s[34:35]
	v_lshl_add_u64 v[170:171], v[168:169], 0, v[2:3]
	v_exp_f32_e32 v128, v128
	v_exp_f32_e32 v129, v129
	v_exp_f32_e32 v130, v130
	v_exp_f32_e32 v131, v131
	v_exp_f32_e32 v124, v124
	v_exp_f32_e32 v125, v125
	v_exp_f32_e32 v126, v126
	v_exp_f32_e32 v127, v127
	v_exp_f32_e32 v120, v120
	v_exp_f32_e32 v121, v121
	v_exp_f32_e32 v122, v122
	v_exp_f32_e32 v123, v123
	v_exp_f32_e32 v116, v116
	v_exp_f32_e32 v117, v117
	v_exp_f32_e32 v118, v118
	v_exp_f32_e32 v119, v119
	v_add_f32_e32 v128, 1.0, v128
	v_add_f32_e32 v129, 1.0, v129
	v_add_f32_e32 v130, 1.0, v130
	v_add_f32_e32 v131, 1.0, v131
	v_add_f32_e32 v124, 1.0, v124
	v_add_f32_e32 v125, 1.0, v125
	v_add_f32_e32 v126, 1.0, v126
	v_add_f32_e32 v127, 1.0, v127
	v_add_f32_e32 v120, 1.0, v120
	v_add_f32_e32 v121, 1.0, v121
	v_add_f32_e32 v122, 1.0, v122
	v_add_f32_e32 v123, 1.0, v123
	v_add_f32_e32 v116, 1.0, v116
	v_add_f32_e32 v117, 1.0, v117
	v_add_f32_e32 v118, 1.0, v118
	v_add_f32_e32 v119, 1.0, v119
	v_rcp_f32_e32 v128, v128
	v_rcp_f32_e32 v129, v129
	v_rcp_f32_e32 v130, v130
	v_rcp_f32_e32 v131, v131
	v_rcp_f32_e32 v124, v124
	v_rcp_f32_e32 v125, v125
	v_rcp_f32_e32 v126, v126
	v_rcp_f32_e32 v127, v127
	v_rcp_f32_e32 v120, v120
	v_rcp_f32_e32 v121, v121
	v_rcp_f32_e32 v122, v122
	v_rcp_f32_e32 v123, v123
	v_rcp_f32_e32 v116, v116
	v_rcp_f32_e32 v117, v117
	v_rcp_f32_e32 v118, v118
	v_rcp_f32_e32 v119, v119
	v_add_u32_e32 v128, 0xc4820000, v128
	v_add_u32_e32 v129, 0xc4820000, v129
	v_add_u32_e32 v130, 0xc4820000, v130
	v_add_u32_e32 v131, 0xc4820000, v131
	v_add_u32_e32 v124, 0xc4820000, v124
	v_add_u32_e32 v125, 0xc4820000, v125
	v_add_u32_e32 v126, 0xc4820000, v126
	v_add_u32_e32 v127, 0xc4820000, v127
	v_add_u32_e32 v120, 0xc4820000, v120
	v_add_u32_e32 v121, 0xc4820000, v121
	v_add_u32_e32 v122, 0xc4820000, v122
	v_add_u32_e32 v123, 0xc4820000, v123
	v_add_u32_e32 v116, 0xc4820000, v116
	v_add_u32_e32 v117, 0xc4820000, v117
	v_add_u32_e32 v118, 0xc4820000, v118
	v_add_u32_e32 v119, 0xc4820000, v119
	v_ashr_pk_u8_i32 v128, v128, v129, 18
	v_ashr_pk_u8_i32 v130, v130, v131, 18
	v_ashr_pk_u8_i32 v124, v124, v125, 18
	v_ashr_pk_u8_i32 v126, v126, v127, 18
	v_ashr_pk_u8_i32 v120, v120, v121, 18
	v_ashr_pk_u8_i32 v122, v122, v123, 18
	v_ashr_pk_u8_i32 v116, v116, v117, 18
	v_ashr_pk_u8_i32 v118, v118, v119, 18
	v_and_b32_e32 v128, 0xffff, v128
	v_lshl_or_b32 v164, v130, 16, v128
	v_and_b32_e32 v124, 0xffff, v124
	v_lshl_or_b32 v165, v126, 16, v124
	v_and_b32_e32 v120, 0xffff, v120
	v_lshl_or_b32 v166, v122, 16, v120
	v_and_b32_e32 v116, 0xffff, v116
	v_lshl_or_b32 v167, v118, 16, v116
	global_store_dwordx4 v[170:171], v[164:167], off
	s_and_b64 vcc, exec, s[40:41]
	s_mov_b64 s[26:27], -1
	s_cbranch_vccz .LBB0_975

.LBB0_857:
	s_waitcnt lgkmcnt(0)
	v_fmamk_f32 v96, v96, 0xbfb8aa3b, v136
	v_fmamk_f32 v97, v97, 0xbfb8aa3b, v137
	v_fmamk_f32 v98, v98, 0xbfb8aa3b, v138
	v_fmamk_f32 v99, v99, 0xbfb8aa3b, v139
	v_fmamk_f32 v92, v92, 0xbfb8aa3b, v132
	v_fmamk_f32 v93, v93, 0xbfb8aa3b, v133
	v_fmamk_f32 v94, v94, 0xbfb8aa3b, v134
	v_fmamk_f32 v95, v95, 0xbfb8aa3b, v135
	v_fmamk_f32 v88, v88, 0xbfb8aa3b, v140
	v_fmamk_f32 v89, v89, 0xbfb8aa3b, v141
	v_fmamk_f32 v90, v90, 0xbfb8aa3b, v142
	v_fmamk_f32 v91, v91, 0xbfb8aa3b, v143
	v_fmamk_f32 v84, v84, 0xbfb8aa3b, v144
	v_fmamk_f32 v85, v85, 0xbfb8aa3b, v145
	v_fmamk_f32 v86, v86, 0xbfb8aa3b, v146
	v_fmamk_f32 v87, v87, 0xbfb8aa3b, v147
	v_mov_b32_e32 v118, v150
	s_add_i32 s19, s87, -11
	s_lshr_b32 s20, s19, 2
	v_mov_b32_e32 v136, s20
	v_mov_b32_e32 v137, v3
	v_mad_i64_i32 v[136:137], s[20:21], v224, 3, v[136:137]
	v_lshlrev_b64 v[136:137], 10, v[136:137]
	s_lshl_b32 s19, s19, 8
	s_and_b32 s34, s19, 0x300
	v_lshl_add_u64 v[136:137], s[46:47], 0, v[136:137]
	v_lshl_add_u64 v[136:137], v[136:137], 0, s[34:35]
	v_lshl_add_u64 v[138:139], v[136:137], 0, v[2:3]
	v_exp_f32_e32 v96, v96
	v_exp_f32_e32 v97, v97
	v_exp_f32_e32 v98, v98
	v_exp_f32_e32 v99, v99
	v_exp_f32_e32 v92, v92
	v_exp_f32_e32 v93, v93
	v_exp_f32_e32 v94, v94
	v_exp_f32_e32 v95, v95
	v_exp_f32_e32 v88, v88
	v_exp_f32_e32 v89, v89
	v_exp_f32_e32 v90, v90
	v_exp_f32_e32 v91, v91
	v_exp_f32_e32 v84, v84
	v_exp_f32_e32 v85, v85
	v_exp_f32_e32 v86, v86
	v_exp_f32_e32 v87, v87
	v_add_f32_e32 v96, 1.0, v96
	v_add_f32_e32 v97, 1.0, v97
	v_add_f32_e32 v98, 1.0, v98
	v_add_f32_e32 v99, 1.0, v99
	v_add_f32_e32 v92, 1.0, v92
	v_add_f32_e32 v93, 1.0, v93
	v_add_f32_e32 v94, 1.0, v94
	v_add_f32_e32 v95, 1.0, v95
	v_add_f32_e32 v88, 1.0, v88
	v_add_f32_e32 v89, 1.0, v89
	v_add_f32_e32 v90, 1.0, v90
	v_add_f32_e32 v91, 1.0, v91
	v_add_f32_e32 v84, 1.0, v84
	v_add_f32_e32 v85, 1.0, v85
	v_add_f32_e32 v86, 1.0, v86
	v_add_f32_e32 v87, 1.0, v87
	v_rcp_f32_e32 v96, v96
	v_rcp_f32_e32 v97, v97
	v_rcp_f32_e32 v98, v98
	v_rcp_f32_e32 v99, v99
	v_rcp_f32_e32 v92, v92
	v_rcp_f32_e32 v93, v93
	v_rcp_f32_e32 v94, v94
	v_rcp_f32_e32 v95, v95
	v_rcp_f32_e32 v88, v88
	v_rcp_f32_e32 v89, v89
	v_rcp_f32_e32 v90, v90
	v_rcp_f32_e32 v91, v91
	v_rcp_f32_e32 v84, v84
	v_rcp_f32_e32 v85, v85
	v_rcp_f32_e32 v86, v86
	v_rcp_f32_e32 v87, v87
	v_add_u32_e32 v96, 0xc4820000, v96
	v_add_u32_e32 v97, 0xc4820000, v97
	v_add_u32_e32 v98, 0xc4820000, v98
	v_add_u32_e32 v99, 0xc4820000, v99
	v_add_u32_e32 v92, 0xc4820000, v92
	v_add_u32_e32 v93, 0xc4820000, v93
	v_add_u32_e32 v94, 0xc4820000, v94
	v_add_u32_e32 v95, 0xc4820000, v95
	v_add_u32_e32 v88, 0xc4820000, v88
	v_add_u32_e32 v89, 0xc4820000, v89
	v_add_u32_e32 v90, 0xc4820000, v90
	v_add_u32_e32 v91, 0xc4820000, v91
	v_add_u32_e32 v84, 0xc4820000, v84
	v_add_u32_e32 v85, 0xc4820000, v85
	v_add_u32_e32 v86, 0xc4820000, v86
	v_add_u32_e32 v87, 0xc4820000, v87
	v_ashr_pk_u8_i32 v96, v96, v97, 18
	v_ashr_pk_u8_i32 v98, v98, v99, 18
	v_ashr_pk_u8_i32 v92, v92, v93, 18
	v_ashr_pk_u8_i32 v94, v94, v95, 18
	v_ashr_pk_u8_i32 v88, v88, v89, 18
	v_ashr_pk_u8_i32 v90, v90, v91, 18
	v_ashr_pk_u8_i32 v84, v84, v85, 18
	v_ashr_pk_u8_i32 v86, v86, v87, 18
	v_and_b32_e32 v96, 0xffff, v96
	v_lshl_or_b32 v132, v98, 16, v96
	v_and_b32_e32 v92, 0xffff, v92
	v_lshl_or_b32 v133, v94, 16, v92
	v_and_b32_e32 v88, 0xffff, v88
	v_lshl_or_b32 v134, v90, 16, v88
	v_and_b32_e32 v84, 0xffff, v84
	v_lshl_or_b32 v135, v86, 16, v84
	global_store_dwordx4 v[138:139], v[132:135], off
	s_and_b64 vcc, exec, s[40:41]
	s_mov_b64 s[26:27], -1
	s_cbranch_vccz .LBB0_1025

.LBB0_859:
	s_waitcnt lgkmcnt(0)
	v_fmamk_f32 v80, v80, 0xbfb8aa3b, v104
	v_fmamk_f32 v81, v81, 0xbfb8aa3b, v105
	v_fmamk_f32 v82, v82, 0xbfb8aa3b, v106
	v_fmamk_f32 v83, v83, 0xbfb8aa3b, v107
	v_fmamk_f32 v76, v76, 0xbfb8aa3b, v100
	v_fmamk_f32 v77, v77, 0xbfb8aa3b, v101
	v_fmamk_f32 v78, v78, 0xbfb8aa3b, v102
	v_fmamk_f32 v79, v79, 0xbfb8aa3b, v103
	v_fmamk_f32 v72, v72, 0xbfb8aa3b, v108
	v_fmamk_f32 v73, v73, 0xbfb8aa3b, v109
	v_fmamk_f32 v74, v74, 0xbfb8aa3b, v110
	v_fmamk_f32 v75, v75, 0xbfb8aa3b, v111
	v_fmamk_f32 v68, v68, 0xbfb8aa3b, v112
	v_fmamk_f32 v69, v69, 0xbfb8aa3b, v113
	v_fmamk_f32 v70, v70, 0xbfb8aa3b, v114
	v_fmamk_f32 v71, v71, 0xbfb8aa3b, v115
	v_mov_b32_e32 v142, v118
	s_add_i32 s19, s87, -11
	s_lshr_b32 s20, s19, 2
	v_mov_b32_e32 v104, s20
	v_mov_b32_e32 v105, v3
	v_mad_i64_i32 v[104:105], s[20:21], v222, 3, v[104:105]
	v_lshlrev_b64 v[104:105], 10, v[104:105]
	s_lshl_b32 s19, s19, 8
	s_and_b32 s34, s19, 0x300
	v_lshl_add_u64 v[104:105], s[46:47], 0, v[104:105]
	v_lshl_add_u64 v[104:105], v[104:105], 0, s[34:35]
	v_lshl_add_u64 v[106:107], v[104:105], 0, v[2:3]
	v_exp_f32_e32 v80, v80
	v_exp_f32_e32 v81, v81
	v_exp_f32_e32 v82, v82
	v_exp_f32_e32 v83, v83
	v_exp_f32_e32 v76, v76
	v_exp_f32_e32 v77, v77
	v_exp_f32_e32 v78, v78
	v_exp_f32_e32 v79, v79
	v_exp_f32_e32 v72, v72
	v_exp_f32_e32 v73, v73
	v_exp_f32_e32 v74, v74
	v_exp_f32_e32 v75, v75
	v_exp_f32_e32 v68, v68
	v_exp_f32_e32 v69, v69
	v_exp_f32_e32 v70, v70
	v_exp_f32_e32 v71, v71
	v_add_f32_e32 v80, 1.0, v80
	v_add_f32_e32 v81, 1.0, v81
	v_add_f32_e32 v82, 1.0, v82
	v_add_f32_e32 v83, 1.0, v83
	v_add_f32_e32 v76, 1.0, v76
	v_add_f32_e32 v77, 1.0, v77
	v_add_f32_e32 v78, 1.0, v78
	v_add_f32_e32 v79, 1.0, v79
	v_add_f32_e32 v72, 1.0, v72
	v_add_f32_e32 v73, 1.0, v73
	v_add_f32_e32 v74, 1.0, v74
	v_add_f32_e32 v75, 1.0, v75
	v_add_f32_e32 v68, 1.0, v68
	v_add_f32_e32 v69, 1.0, v69
	v_add_f32_e32 v70, 1.0, v70
	v_add_f32_e32 v71, 1.0, v71
	v_rcp_f32_e32 v80, v80
	v_rcp_f32_e32 v81, v81
	v_rcp_f32_e32 v82, v82
	v_rcp_f32_e32 v83, v83
	v_rcp_f32_e32 v76, v76
	v_rcp_f32_e32 v77, v77
	v_rcp_f32_e32 v78, v78
	v_rcp_f32_e32 v79, v79
	v_rcp_f32_e32 v72, v72
	v_rcp_f32_e32 v73, v73
	v_rcp_f32_e32 v74, v74
	v_rcp_f32_e32 v75, v75
	v_rcp_f32_e32 v68, v68
	v_rcp_f32_e32 v69, v69
	v_rcp_f32_e32 v70, v70
	v_rcp_f32_e32 v71, v71
	v_add_u32_e32 v80, 0xc4820000, v80
	v_add_u32_e32 v81, 0xc4820000, v81
	v_add_u32_e32 v82, 0xc4820000, v82
	v_add_u32_e32 v83, 0xc4820000, v83
	v_add_u32_e32 v76, 0xc4820000, v76
	v_add_u32_e32 v77, 0xc4820000, v77
	v_add_u32_e32 v78, 0xc4820000, v78
	v_add_u32_e32 v79, 0xc4820000, v79
	v_add_u32_e32 v72, 0xc4820000, v72
	v_add_u32_e32 v73, 0xc4820000, v73
	v_add_u32_e32 v74, 0xc4820000, v74
	v_add_u32_e32 v75, 0xc4820000, v75
	v_add_u32_e32 v68, 0xc4820000, v68
	v_add_u32_e32 v69, 0xc4820000, v69
	v_add_u32_e32 v70, 0xc4820000, v70
	v_add_u32_e32 v71, 0xc4820000, v71
	v_ashr_pk_u8_i32 v80, v80, v81, 18
	v_ashr_pk_u8_i32 v82, v82, v83, 18
	v_ashr_pk_u8_i32 v76, v76, v77, 18
	v_ashr_pk_u8_i32 v78, v78, v79, 18
	v_ashr_pk_u8_i32 v72, v72, v73, 18
	v_ashr_pk_u8_i32 v74, v74, v75, 18
	v_ashr_pk_u8_i32 v68, v68, v69, 18
	v_ashr_pk_u8_i32 v70, v70, v71, 18
	v_and_b32_e32 v80, 0xffff, v80
	v_lshl_or_b32 v100, v82, 16, v80
	v_and_b32_e32 v76, 0xffff, v76
	v_lshl_or_b32 v101, v78, 16, v76
	v_and_b32_e32 v72, 0xffff, v72
	v_lshl_or_b32 v102, v74, 16, v72
	v_and_b32_e32 v68, 0xffff, v68
	v_lshl_or_b32 v103, v70, 16, v68
	global_store_dwordx4 v[106:107], v[100:103], off

.LBB0_885:
	s_waitcnt lgkmcnt(1)
	s_waitcnt lgkmcnt(0)
	v_fmamk_f32 v64, v64, 0xbfb8aa3b, v120
	v_fmamk_f32 v65, v65, 0xbfb8aa3b, v121
	v_fmamk_f32 v66, v66, 0xbfb8aa3b, v122
	v_fmamk_f32 v67, v67, 0xbfb8aa3b, v123
	v_fmamk_f32 v60, v60, 0xbfb8aa3b, v116
	v_fmamk_f32 v61, v61, 0xbfb8aa3b, v117
	v_fmamk_f32 v62, v62, 0xbfb8aa3b, v118
	v_fmamk_f32 v63, v63, 0xbfb8aa3b, v119
	v_fmamk_f32 v56, v56, 0xbfb8aa3b, v124
	v_fmamk_f32 v57, v57, 0xbfb8aa3b, v125
	v_fmamk_f32 v58, v58, 0xbfb8aa3b, v126
	v_fmamk_f32 v59, v59, 0xbfb8aa3b, v127
	v_fmamk_f32 v52, v52, 0xbfb8aa3b, v128
	v_fmamk_f32 v53, v53, 0xbfb8aa3b, v129
	v_fmamk_f32 v54, v54, 0xbfb8aa3b, v130
	v_fmamk_f32 v55, v55, 0xbfb8aa3b, v131
	v_mov_b32_e32 v133, v142
	s_add_i32 s19, s87, -11
	s_lshr_b32 s20, s19, 2
	v_mov_b32_e32 v120, s20
	v_mov_b32_e32 v121, v3
	v_mad_i64_i32 v[120:121], s[20:21], v138, 3, v[120:121]
	v_lshlrev_b64 v[120:121], 10, v[120:121]
	s_lshl_b32 s19, s19, 8
	s_and_b32 s34, s19, 0x300
	v_lshl_add_u64 v[120:121], s[46:47], 0, v[120:121]
	v_lshl_add_u64 v[120:121], v[120:121], 0, s[34:35]
	v_lshl_add_u64 v[122:123], v[120:121], 0, v[2:3]
	v_exp_f32_e32 v64, v64
	v_exp_f32_e32 v65, v65
	v_exp_f32_e32 v66, v66
	v_exp_f32_e32 v67, v67
	v_exp_f32_e32 v60, v60
	v_exp_f32_e32 v61, v61
	v_exp_f32_e32 v62, v62
	v_exp_f32_e32 v63, v63
	v_exp_f32_e32 v56, v56
	v_exp_f32_e32 v57, v57
	v_exp_f32_e32 v58, v58
	v_exp_f32_e32 v59, v59
	v_exp_f32_e32 v52, v52
	v_exp_f32_e32 v53, v53
	v_exp_f32_e32 v54, v54
	v_exp_f32_e32 v55, v55
	v_add_f32_e32 v64, 1.0, v64
	v_add_f32_e32 v65, 1.0, v65
	v_add_f32_e32 v66, 1.0, v66
	v_add_f32_e32 v67, 1.0, v67
	v_add_f32_e32 v60, 1.0, v60
	v_add_f32_e32 v61, 1.0, v61
	v_add_f32_e32 v62, 1.0, v62
	v_add_f32_e32 v63, 1.0, v63
	v_add_f32_e32 v56, 1.0, v56
	v_add_f32_e32 v57, 1.0, v57
	v_add_f32_e32 v58, 1.0, v58
	v_add_f32_e32 v59, 1.0, v59
	v_add_f32_e32 v52, 1.0, v52
	v_add_f32_e32 v53, 1.0, v53
	v_add_f32_e32 v54, 1.0, v54
	v_add_f32_e32 v55, 1.0, v55
	v_rcp_f32_e32 v64, v64
	v_rcp_f32_e32 v65, v65
	v_rcp_f32_e32 v66, v66
	v_rcp_f32_e32 v67, v67
	v_rcp_f32_e32 v60, v60
	v_rcp_f32_e32 v61, v61
	v_rcp_f32_e32 v62, v62
	v_rcp_f32_e32 v63, v63
	v_rcp_f32_e32 v56, v56
	v_rcp_f32_e32 v57, v57
	v_rcp_f32_e32 v58, v58
	v_rcp_f32_e32 v59, v59
	v_rcp_f32_e32 v52, v52
	v_rcp_f32_e32 v53, v53
	v_rcp_f32_e32 v54, v54
	v_rcp_f32_e32 v55, v55
	v_add_u32_e32 v64, 0xc4820000, v64
	v_add_u32_e32 v65, 0xc4820000, v65
	v_add_u32_e32 v66, 0xc4820000, v66
	v_add_u32_e32 v67, 0xc4820000, v67
	v_add_u32_e32 v60, 0xc4820000, v60
	v_add_u32_e32 v61, 0xc4820000, v61
	v_add_u32_e32 v62, 0xc4820000, v62
	v_add_u32_e32 v63, 0xc4820000, v63
	v_add_u32_e32 v56, 0xc4820000, v56
	v_add_u32_e32 v57, 0xc4820000, v57
	v_add_u32_e32 v58, 0xc4820000, v58
	v_add_u32_e32 v59, 0xc4820000, v59
	v_add_u32_e32 v52, 0xc4820000, v52
	v_add_u32_e32 v53, 0xc4820000, v53
	v_add_u32_e32 v54, 0xc4820000, v54
	v_add_u32_e32 v55, 0xc4820000, v55
	v_ashr_pk_u8_i32 v64, v64, v65, 18
	v_ashr_pk_u8_i32 v66, v66, v67, 18
	v_ashr_pk_u8_i32 v60, v60, v61, 18
	v_ashr_pk_u8_i32 v62, v62, v63, 18
	v_ashr_pk_u8_i32 v56, v56, v57, 18
	v_ashr_pk_u8_i32 v58, v58, v59, 18
	v_ashr_pk_u8_i32 v52, v52, v53, 18
	v_ashr_pk_u8_i32 v54, v54, v55, 18
	v_and_b32_e32 v64, 0xffff, v64
	v_lshl_or_b32 v116, v66, 16, v64
	v_and_b32_e32 v60, 0xffff, v60
	v_lshl_or_b32 v117, v62, 16, v60
	v_and_b32_e32 v56, 0xffff, v56
	v_lshl_or_b32 v118, v58, 16, v56
	v_and_b32_e32 v52, 0xffff, v52
	v_lshl_or_b32 v119, v54, 16, v52
	global_store_dwordx4 v[122:123], v[116:119], off
	s_and_b64 vcc, exec, s[40:41]
	s_mov_b64 s[26:27], -1
	s_cbranch_vccz .LBB0_950

.LBB0_887:
	s_waitcnt lgkmcnt(1)
	s_waitcnt lgkmcnt(0)
	v_fmamk_f32 v48, v48, 0xbfb8aa3b, v104
	v_fmamk_f32 v49, v49, 0xbfb8aa3b, v105
	v_fmamk_f32 v50, v50, 0xbfb8aa3b, v106
	v_fmamk_f32 v51, v51, 0xbfb8aa3b, v107
	v_fmamk_f32 v44, v44, 0xbfb8aa3b, v100
	v_fmamk_f32 v45, v45, 0xbfb8aa3b, v101
	v_fmamk_f32 v46, v46, 0xbfb8aa3b, v102
	v_fmamk_f32 v47, v47, 0xbfb8aa3b, v103
	v_fmamk_f32 v40, v40, 0xbfb8aa3b, v108
	v_fmamk_f32 v41, v41, 0xbfb8aa3b, v109
	v_fmamk_f32 v42, v42, 0xbfb8aa3b, v110
	v_fmamk_f32 v43, v43, 0xbfb8aa3b, v111
	v_fmamk_f32 v36, v36, 0xbfb8aa3b, v112
	v_fmamk_f32 v37, v37, 0xbfb8aa3b, v113
	v_fmamk_f32 v38, v38, 0xbfb8aa3b, v114
	v_fmamk_f32 v39, v39, 0xbfb8aa3b, v115
	v_mov_b32_e32 v54, v133
	s_add_i32 s19, s87, -11
	s_lshr_b32 s20, s19, 2
	v_mov_b32_e32 v104, s20
	v_mov_b32_e32 v105, v3
	v_mad_i64_i32 v[104:105], s[20:21], v136, 3, v[104:105]
	v_lshlrev_b64 v[104:105], 10, v[104:105]
	s_lshl_b32 s19, s19, 8
	s_and_b32 s34, s19, 0x300
	v_lshl_add_u64 v[104:105], s[46:47], 0, v[104:105]
	v_lshl_add_u64 v[104:105], v[104:105], 0, s[34:35]
	v_lshl_add_u64 v[106:107], v[104:105], 0, v[2:3]
	v_exp_f32_e32 v48, v48
	v_exp_f32_e32 v49, v49
	v_exp_f32_e32 v50, v50
	v_exp_f32_e32 v51, v51
	v_exp_f32_e32 v44, v44
	v_exp_f32_e32 v45, v45
	v_exp_f32_e32 v46, v46
	v_exp_f32_e32 v47, v47
	v_exp_f32_e32 v40, v40
	v_exp_f32_e32 v41, v41
	v_exp_f32_e32 v42, v42
	v_exp_f32_e32 v43, v43
	v_exp_f32_e32 v36, v36
	v_exp_f32_e32 v37, v37
	v_exp_f32_e32 v38, v38
	v_exp_f32_e32 v39, v39
	v_add_f32_e32 v48, 1.0, v48
	v_add_f32_e32 v49, 1.0, v49
	v_add_f32_e32 v50, 1.0, v50
	v_add_f32_e32 v51, 1.0, v51
	v_add_f32_e32 v44, 1.0, v44
	v_add_f32_e32 v45, 1.0, v45
	v_add_f32_e32 v46, 1.0, v46
	v_add_f32_e32 v47, 1.0, v47
	v_add_f32_e32 v40, 1.0, v40
	v_add_f32_e32 v41, 1.0, v41
	v_add_f32_e32 v42, 1.0, v42
	v_add_f32_e32 v43, 1.0, v43
	v_add_f32_e32 v36, 1.0, v36
	v_add_f32_e32 v37, 1.0, v37
	v_add_f32_e32 v38, 1.0, v38
	v_add_f32_e32 v39, 1.0, v39
	v_rcp_f32_e32 v48, v48
	v_rcp_f32_e32 v49, v49
	v_rcp_f32_e32 v50, v50
	v_rcp_f32_e32 v51, v51
	v_rcp_f32_e32 v44, v44
	v_rcp_f32_e32 v45, v45
	v_rcp_f32_e32 v46, v46
	v_rcp_f32_e32 v47, v47
	v_rcp_f32_e32 v40, v40
	v_rcp_f32_e32 v41, v41
	v_rcp_f32_e32 v42, v42
	v_rcp_f32_e32 v43, v43
	v_rcp_f32_e32 v36, v36
	v_rcp_f32_e32 v37, v37
	v_rcp_f32_e32 v38, v38
	v_rcp_f32_e32 v39, v39
	v_add_u32_e32 v48, 0xc4820000, v48
	v_add_u32_e32 v49, 0xc4820000, v49
	v_add_u32_e32 v50, 0xc4820000, v50
	v_add_u32_e32 v51, 0xc4820000, v51
	v_add_u32_e32 v44, 0xc4820000, v44
	v_add_u32_e32 v45, 0xc4820000, v45
	v_add_u32_e32 v46, 0xc4820000, v46
	v_add_u32_e32 v47, 0xc4820000, v47
	v_add_u32_e32 v40, 0xc4820000, v40
	v_add_u32_e32 v41, 0xc4820000, v41
	v_add_u32_e32 v42, 0xc4820000, v42
	v_add_u32_e32 v43, 0xc4820000, v43
	v_add_u32_e32 v36, 0xc4820000, v36
	v_add_u32_e32 v37, 0xc4820000, v37
	v_add_u32_e32 v38, 0xc4820000, v38
	v_add_u32_e32 v39, 0xc4820000, v39
	v_ashr_pk_u8_i32 v48, v48, v49, 18
	v_ashr_pk_u8_i32 v50, v50, v51, 18
	v_ashr_pk_u8_i32 v44, v44, v45, 18
	v_ashr_pk_u8_i32 v46, v46, v47, 18
	v_ashr_pk_u8_i32 v40, v40, v41, 18
	v_ashr_pk_u8_i32 v42, v42, v43, 18
	v_ashr_pk_u8_i32 v36, v36, v37, 18
	v_ashr_pk_u8_i32 v38, v38, v39, 18
	v_and_b32_e32 v48, 0xffff, v48
	v_lshl_or_b32 v100, v50, 16, v48
	v_and_b32_e32 v44, 0xffff, v44
	v_lshl_or_b32 v101, v46, 16, v44
	v_and_b32_e32 v40, 0xffff, v40
	v_lshl_or_b32 v102, v42, 16, v40
	v_and_b32_e32 v36, 0xffff, v36
	v_lshl_or_b32 v103, v38, 16, v36
	global_store_dwordx4 v[106:107], v[100:103], off
	s_and_b64 vcc, exec, s[40:41]
	s_mov_b64 s[26:27], -1
	s_cbranch_vccz .LBB0_1000

.LBB0_889:
	s_waitcnt lgkmcnt(1)
	s_waitcnt lgkmcnt(0)
	v_fmamk_f32 v32, v32, 0xbfb8aa3b, v88
	v_fmamk_f32 v33, v33, 0xbfb8aa3b, v89
	v_fmamk_f32 v34, v34, 0xbfb8aa3b, v90
	v_fmamk_f32 v35, v35, 0xbfb8aa3b, v91
	v_fmamk_f32 v28, v28, 0xbfb8aa3b, v84
	v_fmamk_f32 v29, v29, 0xbfb8aa3b, v85
	v_fmamk_f32 v30, v30, 0xbfb8aa3b, v86
	v_fmamk_f32 v31, v31, 0xbfb8aa3b, v87
	v_fmamk_f32 v24, v24, 0xbfb8aa3b, v92
	v_fmamk_f32 v25, v25, 0xbfb8aa3b, v93
	v_fmamk_f32 v26, v26, 0xbfb8aa3b, v94
	v_fmamk_f32 v27, v27, 0xbfb8aa3b, v95
	v_fmamk_f32 v20, v20, 0xbfb8aa3b, v96
	v_fmamk_f32 v21, v21, 0xbfb8aa3b, v97
	v_fmamk_f32 v22, v22, 0xbfb8aa3b, v98
	v_fmamk_f32 v23, v23, 0xbfb8aa3b, v99
	v_mov_b32_e32 v38, v54
	s_add_i32 s19, s87, -11
	s_lshr_b32 s20, s19, 2
	v_mov_b32_e32 v88, s20
	v_mov_b32_e32 v89, v3
	v_mad_i64_i32 v[88:89], s[20:21], v134, 3, v[88:89]
	v_lshlrev_b64 v[88:89], 10, v[88:89]
	s_lshl_b32 s19, s19, 8
	s_and_b32 s34, s19, 0x300
	v_lshl_add_u64 v[88:89], s[46:47], 0, v[88:89]
	v_lshl_add_u64 v[88:89], v[88:89], 0, s[34:35]
	v_lshl_add_u64 v[90:91], v[88:89], 0, v[2:3]
	v_exp_f32_e32 v32, v32
	v_exp_f32_e32 v33, v33
	v_exp_f32_e32 v34, v34
	v_exp_f32_e32 v35, v35
	v_exp_f32_e32 v28, v28
	v_exp_f32_e32 v29, v29
	v_exp_f32_e32 v30, v30
	v_exp_f32_e32 v31, v31
	v_exp_f32_e32 v24, v24
	v_exp_f32_e32 v25, v25
	v_exp_f32_e32 v26, v26
	v_exp_f32_e32 v27, v27
	v_exp_f32_e32 v20, v20
	v_exp_f32_e32 v21, v21
	v_exp_f32_e32 v22, v22
	v_exp_f32_e32 v23, v23
	v_add_f32_e32 v32, 1.0, v32
	v_add_f32_e32 v33, 1.0, v33
	v_add_f32_e32 v34, 1.0, v34
	v_add_f32_e32 v35, 1.0, v35
	v_add_f32_e32 v28, 1.0, v28
	v_add_f32_e32 v29, 1.0, v29
	v_add_f32_e32 v30, 1.0, v30
	v_add_f32_e32 v31, 1.0, v31
	v_add_f32_e32 v24, 1.0, v24
	v_add_f32_e32 v25, 1.0, v25
	v_add_f32_e32 v26, 1.0, v26
	v_add_f32_e32 v27, 1.0, v27
	v_add_f32_e32 v20, 1.0, v20
	v_add_f32_e32 v21, 1.0, v21
	v_add_f32_e32 v22, 1.0, v22
	v_add_f32_e32 v23, 1.0, v23
	v_rcp_f32_e32 v32, v32
	v_rcp_f32_e32 v33, v33
	v_rcp_f32_e32 v34, v34
	v_rcp_f32_e32 v35, v35
	v_rcp_f32_e32 v28, v28
	v_rcp_f32_e32 v29, v29
	v_rcp_f32_e32 v30, v30
	v_rcp_f32_e32 v31, v31
	v_rcp_f32_e32 v24, v24
	v_rcp_f32_e32 v25, v25
	v_rcp_f32_e32 v26, v26
	v_rcp_f32_e32 v27, v27
	v_rcp_f32_e32 v20, v20
	v_rcp_f32_e32 v21, v21
	v_rcp_f32_e32 v22, v22
	v_rcp_f32_e32 v23, v23
	v_add_u32_e32 v32, 0xc4820000, v32
	v_add_u32_e32 v33, 0xc4820000, v33
	v_add_u32_e32 v34, 0xc4820000, v34
	v_add_u32_e32 v35, 0xc4820000, v35
	v_add_u32_e32 v28, 0xc4820000, v28
	v_add_u32_e32 v29, 0xc4820000, v29
	v_add_u32_e32 v30, 0xc4820000, v30
	v_add_u32_e32 v31, 0xc4820000, v31
	v_add_u32_e32 v24, 0xc4820000, v24
	v_add_u32_e32 v25, 0xc4820000, v25
	v_add_u32_e32 v26, 0xc4820000, v26
	v_add_u32_e32 v27, 0xc4820000, v27
	v_add_u32_e32 v20, 0xc4820000, v20
	v_add_u32_e32 v21, 0xc4820000, v21
	v_add_u32_e32 v22, 0xc4820000, v22
	v_add_u32_e32 v23, 0xc4820000, v23
	v_ashr_pk_u8_i32 v32, v32, v33, 18
	v_ashr_pk_u8_i32 v34, v34, v35, 18
	v_ashr_pk_u8_i32 v28, v28, v29, 18
	v_ashr_pk_u8_i32 v30, v30, v31, 18
	v_ashr_pk_u8_i32 v24, v24, v25, 18
	v_ashr_pk_u8_i32 v26, v26, v27, 18
	v_ashr_pk_u8_i32 v20, v20, v21, 18
	v_ashr_pk_u8_i32 v22, v22, v23, 18
	v_and_b32_e32 v32, 0xffff, v32
	v_lshl_or_b32 v84, v34, 16, v32
	v_and_b32_e32 v28, 0xffff, v28
	v_lshl_or_b32 v85, v30, 16, v28
	v_and_b32_e32 v24, 0xffff, v24
	v_lshl_or_b32 v86, v26, 16, v24
	v_and_b32_e32 v20, 0xffff, v20
	v_lshl_or_b32 v87, v22, 16, v20
	global_store_dwordx4 v[90:91], v[84:87], off
	s_and_b64 vcc, exec, s[40:41]
	s_mov_b64 s[26:27], -1
	s_cbranch_vccz .LBB0_1050

.LBB0_891:
	s_waitcnt lgkmcnt(1)
	s_waitcnt lgkmcnt(0)
	v_fmamk_f32 v16, v16, 0xbfb8aa3b, v72
	v_fmamk_f32 v17, v17, 0xbfb8aa3b, v73
	v_fmamk_f32 v18, v18, 0xbfb8aa3b, v74
	v_fmamk_f32 v19, v19, 0xbfb8aa3b, v75
	v_fmamk_f32 v12, v12, 0xbfb8aa3b, v68
	v_fmamk_f32 v13, v13, 0xbfb8aa3b, v69
	v_fmamk_f32 v14, v14, 0xbfb8aa3b, v70
	v_fmamk_f32 v15, v15, 0xbfb8aa3b, v71
	v_fmamk_f32 v8, v8, 0xbfb8aa3b, v76
	v_fmamk_f32 v9, v9, 0xbfb8aa3b, v77
	v_fmamk_f32 v10, v10, 0xbfb8aa3b, v78
	v_fmamk_f32 v11, v11, 0xbfb8aa3b, v79
	v_fmamk_f32 v4, v4, 0xbfb8aa3b, v80
	v_fmamk_f32 v5, v5, 0xbfb8aa3b, v81
	v_fmamk_f32 v6, v6, 0xbfb8aa3b, v82
	v_fmamk_f32 v7, v7, 0xbfb8aa3b, v83
	v_mov_b32_e32 v28, v38
	s_add_i32 s87, s87, -11
	s_lshr_b32 s19, s87, 2
	v_mov_b32_e32 v72, s19
	v_mov_b32_e32 v73, v3
	v_mad_i64_i32 v[72:73], s[20:21], v132, 3, v[72:73]
	v_lshlrev_b64 v[72:73], 10, v[72:73]
	s_lshl_b32 s19, s87, 8
	s_and_b32 s34, s19, 0x300
	v_lshl_add_u64 v[72:73], s[46:47], 0, v[72:73]
	v_lshl_add_u64 v[72:73], v[72:73], 0, s[34:35]
	v_lshl_add_u64 v[74:75], v[72:73], 0, v[2:3]
	v_exp_f32_e32 v16, v16
	v_exp_f32_e32 v17, v17
	v_exp_f32_e32 v18, v18
	v_exp_f32_e32 v19, v19
	v_exp_f32_e32 v12, v12
	v_exp_f32_e32 v13, v13
	v_exp_f32_e32 v14, v14
	v_exp_f32_e32 v15, v15
	v_exp_f32_e32 v8, v8
	v_exp_f32_e32 v9, v9
	v_exp_f32_e32 v10, v10
	v_exp_f32_e32 v11, v11
	v_exp_f32_e32 v4, v4
	v_exp_f32_e32 v5, v5
	v_exp_f32_e32 v6, v6
	v_exp_f32_e32 v7, v7
	v_add_f32_e32 v16, 1.0, v16
	v_add_f32_e32 v17, 1.0, v17
	v_add_f32_e32 v18, 1.0, v18
	v_add_f32_e32 v19, 1.0, v19
	v_add_f32_e32 v12, 1.0, v12
	v_add_f32_e32 v13, 1.0, v13
	v_add_f32_e32 v14, 1.0, v14
	v_add_f32_e32 v15, 1.0, v15
	v_add_f32_e32 v8, 1.0, v8
	v_add_f32_e32 v9, 1.0, v9
	v_add_f32_e32 v10, 1.0, v10
	v_add_f32_e32 v11, 1.0, v11
	v_add_f32_e32 v4, 1.0, v4
	v_add_f32_e32 v5, 1.0, v5
	v_add_f32_e32 v6, 1.0, v6
	v_add_f32_e32 v7, 1.0, v7
	v_rcp_f32_e32 v16, v16
	v_rcp_f32_e32 v17, v17
	v_rcp_f32_e32 v18, v18
	v_rcp_f32_e32 v19, v19
	v_rcp_f32_e32 v12, v12
	v_rcp_f32_e32 v13, v13
	v_rcp_f32_e32 v14, v14
	v_rcp_f32_e32 v15, v15
	v_rcp_f32_e32 v8, v8
	v_rcp_f32_e32 v9, v9
	v_rcp_f32_e32 v10, v10
	v_rcp_f32_e32 v11, v11
	v_rcp_f32_e32 v4, v4
	v_rcp_f32_e32 v5, v5
	v_rcp_f32_e32 v6, v6
	v_rcp_f32_e32 v7, v7
	v_add_u32_e32 v16, 0xc4820000, v16
	v_add_u32_e32 v17, 0xc4820000, v17
	v_add_u32_e32 v18, 0xc4820000, v18
	v_add_u32_e32 v19, 0xc4820000, v19
	v_add_u32_e32 v12, 0xc4820000, v12
	v_add_u32_e32 v13, 0xc4820000, v13
	v_add_u32_e32 v14, 0xc4820000, v14
	v_add_u32_e32 v15, 0xc4820000, v15
	v_add_u32_e32 v8, 0xc4820000, v8
	v_add_u32_e32 v9, 0xc4820000, v9
	v_add_u32_e32 v10, 0xc4820000, v10
	v_add_u32_e32 v11, 0xc4820000, v11
	v_add_u32_e32 v4, 0xc4820000, v4
	v_add_u32_e32 v5, 0xc4820000, v5
	v_add_u32_e32 v6, 0xc4820000, v6
	v_add_u32_e32 v7, 0xc4820000, v7
	v_ashr_pk_u8_i32 v16, v16, v17, 18
	v_ashr_pk_u8_i32 v18, v18, v19, 18
	v_ashr_pk_u8_i32 v12, v12, v13, 18
	v_ashr_pk_u8_i32 v14, v14, v15, 18
	v_ashr_pk_u8_i32 v8, v8, v9, 18
	v_ashr_pk_u8_i32 v10, v10, v11, 18
	v_ashr_pk_u8_i32 v4, v4, v5, 18
	v_ashr_pk_u8_i32 v6, v6, v7, 18
	v_and_b32_e32 v16, 0xffff, v16
	v_lshl_or_b32 v68, v18, 16, v16
	v_and_b32_e32 v12, 0xffff, v12
	v_lshl_or_b32 v69, v14, 16, v12
	v_and_b32_e32 v8, 0xffff, v8
	v_lshl_or_b32 v70, v10, 16, v8
	v_and_b32_e32 v4, 0xffff, v4
	v_lshl_or_b32 v71, v6, 16, v4
	global_store_dwordx4 v[74:75], v[68:71], off
